# add P11 next-unit gather indices without vmcnt(0) drain at the unit top (opt17)
# speedup vs baseline: 1.0049x; 1.0049x over previous
;     __device__ bool next(int i, Unit& u) const { if (!StaticOrder::next(i >> 1, u)) return false; u.kh = i & 1; return true; }
;     __device__ bool next(int i, Unit& u) const { if (i >= 2) return false; u.pm = 0; u.pn = 0; u.e = 0; u.kh = 0; return true; }
;     __device__ bool next(int i, Unit& u) const { if (!StaticOrder::next(i, u)) return false; u.e = tile_e[u.pm]; return true; }
; template <class Epi, class Sched, bool ALIGN_EPI = false, bool SP2 = false, bool GATHER = false, bool F8 = false>
; __device__ __forceinline__ void gemm_phase(PG8_LAS unsigned char* lds, const Gemm g, const Sched& S, const Epi& E) {
;     ...
;     auto load_gather = [&](const Unit& u, unsigned (&o0)[2], unsigned (&o1)[2]) {
; #pragma unroll
;         for (int i = 0; i < 2; ++i) { int R, C; stage_rc(tid * 16 + i * 8192, R, C); const int t0 = g.gather[u.pm * BM + R], t1 = g.gather[u.pm * BM + HALF + R];
;             o0[i] = (unsigned)(t0 * K + C) * 2u; o1[i] = (unsigned)(t1 * K + C) * 2u; } };
;     ...
;         const bool has_next = S.next(ui + 1, nxt);
;         const char* nA = has_next ? (const char*)((Sched::PAIRS && nxt.kh) ? g.A2 : g.A) + (GATHER ? (size_t)0 : (size_t)nxt.pm * tstep) : cA;
;         if constexpr (GATHER) { if (has_next) load_gather(nxt, gn0, gn1); else { gn0[0] = gc0[0]; gn0[1] = gc0[1]; gn1[0] = gc1[0]; gn1[1] = gc1[1]; } } const char* nB = has_next ? (const char*)((Sched::PAIRS && nxt.kh) ? g.Bt2 : g.Bt) + (size_t)nxt.e * g.bgs + (size_t)nxt.pn * tstep : cB;
.LBB0_1383:
	s_nop 0
	v_cndmask_b32_e64 v2, 0, 1, s[4:5]
	v_cmp_ne_u32_e64 s[0:1], 1, v2
	s_andn2_b64 vcc, exec, s[4:5]
	v_mov_b32_e32 v202, v171
	v_mov_b32_e32 v204, v172
	v_mov_b32_e32 v203, v174
	v_mov_b32_e32 v205, v176
	v_lshrrev_b32_e32 v248, 11, v171
	v_lshrrev_b32_e32 v249, 11, v174
	v_lshrrev_b32_e32 v250, 11, v172
	v_lshrrev_b32_e32 v251, 11, v176
	s_cbranch_vccnz .LBB0_1385
	s_lshl_b32 s37, s52, 8
	s_or_b32 s53, s37, 0x80
	v_or_b32_e32 v2, s37, v1
	v_or_b32_e32 v4, s53, v1
	v_ashrrev_i32_e32 v3, 31, v2
	v_ashrrev_i32_e32 v5, 31, v4
	v_or_b32_e32 v6, s37, v191
	v_or_b32_e32 v8, s53, v191
	v_lshl_add_u64 v[2:3], v[2:3], 2, s[10:11]
	v_lshl_add_u64 v[4:5], v[4:5], 2, s[10:11]
	v_ashrrev_i32_e32 v7, 31, v6
	v_ashrrev_i32_e32 v9, 31, v8
	v_lshl_add_u64 v[6:7], v[6:7], 2, s[10:11]
	v_lshl_add_u64 v[8:9], v[8:9], 2, s[10:11]
	global_load_dword v248, v[2:3], off
	global_load_dword v249, v[4:5], off
	global_load_dword v250, v[6:7], off
	global_load_dword v251, v[8:9], off

; #define PG8_STAGE(bufoff, gbase, voff) do { _Pragma("unroll") for (int _i = 0; _i < 2; ++_i) \
;         __builtin_amdgcn_global_load_lds((const unsigned*)((const char*)(gbase) + (voff)[_i]), (PG8_LAS unsigned*)(lds + (bufoff) + ldsw + _i * 8192), 16, 0, 0); } while (0)
; #define PG8_LDA(dst, b, h) do { _Pragma("unroll") for (int m = 0; m < 4; ++m) _Pragma("unroll") for (int k = 0; k < 2; ++k) dst[m][k] = *(const PG8_LAS bf16x8*)(lds + PG8_SA(b, h) + aoff + m * 2048 + k * KFR); } while (0)
; #define PG8_LDB(dst, b, h) do { _Pragma("unroll") for (int n = 0; n < 2; ++n) _Pragma("unroll") for (int k = 0; k < 2; ++k) dst[n][k] = *(const PG8_LAS bf16x8*)(lds + PG8_SB(b, h) + boff + n * 2048 + k * KFR); } while (0)
; #define PG8_WAIT_V(n) asm volatile("s_waitcnt vmcnt(" #n ")" ::: "memory")
; #define PG8_WAIT_L(n) asm volatile("s_waitcnt lgkmcnt(" #n ")" ::: "memory")
; #define PG8_BAR __builtin_amdgcn_s_barrier()
; #define PG8_SCHED __builtin_amdgcn_sched_barrier(0)
; template <class Epi, class Sched, bool ALIGN_EPI = false, bool SP2 = false, bool GATHER = false, bool F8 = false>
; __device__ __forceinline__ void gemm_phase(PG8_LAS unsigned char* lds, const Gemm g, const Sched& S, const Epi& E) {
;     ...
;             if constexpr (SP2) {
;             PG8_LDB(B0, 0, 0); PG8_LDB(B1, 0, 1); PG8_SCHED; PG8_LDA(At, 0, 0); PG8_STAGE_A(PG8_SA(1, 1), a1, 1, false);
;             PG8_WAIT_V(8); PG8_WAIT_L(0); PG8_BAR; PG8_MMA(0, 0, At, B0); PG8_MMA(0, 1, At, B1); PG8_BAR; PG8_SCHED;
;             PG8_LDA(At, 0, 1); PG8_STAGE(PG8_SB(0, 0), b2, voffB); PG8_STAGE(PG8_SB(0, 1), b2 + hstep, voffB); PG8_STAGE_A(PG8_SA(0, 0), a2, 0, last);
;             PG8_WAIT_V(8); PG8_WAIT_L(0); PG8_BAR; PG8_MMA(1, 0, At, B0); PG8_MMA(1, 1, At, B1); PG8_BAR; PG8_SCHED;
;             PG8_LDB(B0, 1, 0); PG8_LDB(B1, 1, 1); PG8_SCHED; PG8_LDA(At, 1, 0); PG8_STAGE_A(PG8_SA(0, 1), a2, 1, last);
;             PG8_WAIT_V(8); PG8_WAIT_L(0); PG8_BAR; PG8_MMA(0, 0, At, B0); PG8_MMA(0, 1, At, B1); PG8_BAR; PG8_SCHED;
.LBB0_1386:
	ds_read_b128 v[26:29], v197
	ds_read_b128 v[30:33], v197 offset:16
	ds_read_b128 v[18:21], v197 offset:2048
	ds_read_b128 v[22:25], v197 offset:2064
	ds_read_b128 v[10:13], v198
	ds_read_b128 v[14:17], v198 offset:16
	ds_read_b128 v[2:5], v198 offset:2048
	ds_read_b128 v[6:9], v198 offset:2064
	s_add_u32 s4, s64, 0x100
	s_addc_u32 s5, s65, 0
	s_add_u32 s66, s55, s64
	s_addc_u32 s67, s76, s65
	s_cmpk_eq_i32 s64, 0x700
	s_cselect_b64 vcc, -1, 0
	s_and_b64 s[62:63], vcc, exec
	s_cselect_b32 s79, 0, s4
	s_cselect_b32 s78, 0, s5
	s_cselect_b32 s62, s53, s66
	s_cselect_b32 s63, s37, s67
	s_add_u32 s66, s8, s79
	s_addc_u32 s67, s9, s78
	v_lshl_add_u64 v[222:223], v[180:181], 0, s[64:65]
	s_add_i32 m0, s29, 0xc000
	ds_read_b128 v[182:185], v199
	ds_read_b128 v[186:189], v199 offset:16
	ds_read_b128 v[206:209], v199 offset:2048
	ds_read_b128 v[210:213], v199 offset:2064
	ds_read_b128 v[214:217], v199 offset:4096
	ds_read_b128 v[218:221], v199 offset:4112
	ds_read_b128 v[228:231], v199 offset:6144
	ds_read_b128 v[232:235], v199 offset:6160
	global_load_lds_dwordx4 v[222:223], off
	v_lshl_add_u64 v[222:223], v[178:179], 0, s[64:65]
	s_add_i32 m0, s29, 0xe000
	s_nop 0
	global_load_lds_dwordx4 v[222:223], off
	s_waitcnt vmcnt(8)
	s_waitcnt lgkmcnt(0)
	s_barrier
	s_setprio 1
	s_waitcnt lgkmcnt(0)
	v_mfma_scale_f32_16x16x128_f8f6f4 v[158:161], v[26:33], v[182:189], v[158:161], v200, v200 op_sel_hi:[0,0,0]
	v_mfma_scale_f32_16x16x128_f8f6f4 v[154:157], v[18:25], v[182:189], v[154:157], v200, v200 op_sel_hi:[0,0,0]
	v_mfma_scale_f32_16x16x128_f8f6f4 v[142:145], v[26:33], v[206:213], v[142:145], v200, v200 op_sel_hi:[0,0,0]
	v_mfma_scale_f32_16x16x128_f8f6f4 v[134:137], v[18:25], v[206:213], v[134:137], v200, v200 op_sel_hi:[0,0,0]
	v_mfma_scale_f32_16x16x128_f8f6f4 v[126:129], v[26:33], v[214:221], v[126:129], v200, v200 op_sel_hi:[0,0,0]
	v_mfma_scale_f32_16x16x128_f8f6f4 v[118:121], v[18:25], v[214:221], v[118:121], v200, v200 op_sel_hi:[0,0,0]
	v_mfma_scale_f32_16x16x128_f8f6f4 v[110:113], v[26:33], v[228:235], v[110:113], v200, v200 op_sel_hi:[0,0,0]
	v_mfma_scale_f32_16x16x128_f8f6f4 v[102:105], v[18:25], v[228:235], v[102:105], v200, v200 op_sel_hi:[0,0,0]
	s_setprio 0
	s_setprio 1
	v_mfma_scale_f32_16x16x128_f8f6f4 v[150:153], v[10:17], v[182:189], v[150:153], v200, v200 op_sel_hi:[0,0,0]
	v_mfma_scale_f32_16x16x128_f8f6f4 v[146:149], v[2:9], v[182:189], v[146:149], v200, v200 op_sel_hi:[0,0,0]
	v_mfma_scale_f32_16x16x128_f8f6f4 v[138:141], v[10:17], v[206:213], v[138:141], v200, v200 op_sel_hi:[0,0,0]
	v_mfma_scale_f32_16x16x128_f8f6f4 v[130:133], v[2:9], v[206:213], v[130:133], v200, v200 op_sel_hi:[0,0,0]
	v_mfma_scale_f32_16x16x128_f8f6f4 v[122:125], v[10:17], v[214:221], v[122:125], v200, v200 op_sel_hi:[0,0,0]
	v_mfma_scale_f32_16x16x128_f8f6f4 v[114:117], v[2:9], v[214:221], v[114:117], v200, v200 op_sel_hi:[0,0,0]
	v_mfma_scale_f32_16x16x128_f8f6f4 v[106:109], v[10:17], v[228:235], v[106:109], v200, v200 op_sel_hi:[0,0,0]
	v_mfma_scale_f32_16x16x128_f8f6f4 v[98:101], v[2:9], v[228:235], v[98:101], v200, v200 op_sel_hi:[0,0,0]
	s_setprio 0
	s_barrier
	s_add_i32 s64, s7, s25
	v_lshl_add_u64 v[182:183], s[62:63], 0, v[164:165]
	s_mov_b32 m0, s64
	ds_read_b128 v[206:209], v199 offset:16384
	ds_read_b128 v[210:213], v199 offset:16400
	ds_read_b128 v[214:217], v199 offset:18432
	ds_read_b128 v[218:221], v199 offset:18448
	ds_read_b128 v[228:231], v199 offset:20480
	ds_read_b128 v[232:235], v199 offset:20496
	ds_read_b128 v[236:239], v199 offset:22528
	ds_read_b128 v[240:243], v199 offset:22544
	global_load_lds_dwordx4 v[182:183], off
	s_add_i32 m0, s64, 0x2000
	s_add_u32 s64, s62, 0x40000
	v_lshl_add_u64 v[184:185], s[62:63], 0, v[166:167]
	s_addc_u32 s65, s63, 0
	s_add_i32 s78, s71, s25
	global_load_lds_dwordx4 v[184:185], off
	v_lshl_add_u64 v[186:187], s[64:65], 0, v[164:165]
	s_mov_b32 m0, s78
	v_cndmask_b32_e32 v162, v171, v202, vcc
	global_load_lds_dwordx4 v[186:187], off
	v_lshl_add_u64 v[186:187], s[64:65], 0, v[166:167]
	s_add_i32 m0, s78, 0x2000
	s_nop 0
	global_load_lds_dwordx4 v[186:187], off
	s_mov_b32 m0, s29
	v_lshl_add_u64 v[186:187], s[66:67], 0, v[162:163]
	global_load_lds_dwordx4 v162, s[66:67]
	v_cndmask_b32_e32 v162, v172, v204, vcc
	s_mov_b32 m0, s30
	v_lshl_add_u64 v[188:189], s[66:67], 0, v[162:163]
	global_load_lds_dwordx4 v162, s[66:67]
	s_waitcnt vmcnt(8)
	s_waitcnt lgkmcnt(0)
	s_barrier
	s_setprio 1
	s_waitcnt lgkmcnt(0)
	v_mfma_scale_f32_16x16x128_f8f6f4 v[94:97], v[26:33], v[206:213], v[94:97], v200, v200 op_sel_hi:[0,0,0]
	v_mfma_scale_f32_16x16x128_f8f6f4 v[86:89], v[18:25], v[206:213], v[86:89], v200, v200 op_sel_hi:[0,0,0]
	v_mfma_scale_f32_16x16x128_f8f6f4 v[78:81], v[26:33], v[214:221], v[78:81], v200, v200 op_sel_hi:[0,0,0]
	v_mfma_scale_f32_16x16x128_f8f6f4 v[70:73], v[18:25], v[214:221], v[70:73], v200, v200 op_sel_hi:[0,0,0]
	v_mfma_scale_f32_16x16x128_f8f6f4 v[62:65], v[26:33], v[228:235], v[62:65], v200, v200 op_sel_hi:[0,0,0]
	v_mfma_scale_f32_16x16x128_f8f6f4 v[54:57], v[18:25], v[228:235], v[54:57], v200, v200 op_sel_hi:[0,0,0]
	v_mfma_scale_f32_16x16x128_f8f6f4 v[46:49], v[26:33], v[236:243], v[46:49], v200, v200 op_sel_hi:[0,0,0]
	v_mfma_scale_f32_16x16x128_f8f6f4 v[38:41], v[18:25], v[236:243], v[38:41], v200, v200 op_sel_hi:[0,0,0]
	s_setprio 0
	s_setprio 1
	v_mfma_scale_f32_16x16x128_f8f6f4 v[90:93], v[10:17], v[206:213], v[90:93], v200, v200 op_sel_hi:[0,0,0]
	v_mfma_scale_f32_16x16x128_f8f6f4 v[82:85], v[2:9], v[206:213], v[82:85], v200, v200 op_sel_hi:[0,0,0]
	v_mfma_scale_f32_16x16x128_f8f6f4 v[74:77], v[10:17], v[214:221], v[74:77], v200, v200 op_sel_hi:[0,0,0]
	v_mfma_scale_f32_16x16x128_f8f6f4 v[66:69], v[2:9], v[214:221], v[66:69], v200, v200 op_sel_hi:[0,0,0]
	v_mfma_scale_f32_16x16x128_f8f6f4 v[58:61], v[10:17], v[228:235], v[58:61], v200, v200 op_sel_hi:[0,0,0]
	v_mfma_scale_f32_16x16x128_f8f6f4 v[50:53], v[2:9], v[228:235], v[50:53], v200, v200 op_sel_hi:[0,0,0]
	v_mfma_scale_f32_16x16x128_f8f6f4 v[42:45], v[10:17], v[236:243], v[42:45], v200, v200 op_sel_hi:[0,0,0]
	v_mfma_scale_f32_16x16x128_f8f6f4 v[34:37], v[2:9], v[236:243], v[34:37], v200, v200 op_sel_hi:[0,0,0]
	s_setprio 0
	s_barrier
; #define PG8_STAGE(bufoff, gbase, voff) do { _Pragma("unroll") for (int _i = 0; _i < 2; ++_i) \
;         __builtin_amdgcn_global_load_lds((const unsigned*)((const char*)(gbase) + (voff)[_i]), (PG8_LAS unsigned*)(lds + (bufoff) + ldsw + _i * 8192), 16, 0, 0); } while (0)
; #define PG8_LDA(dst, b, h) do { _Pragma("unroll") for (int m = 0; m < 4; ++m) _Pragma("unroll") for (int k = 0; k < 2; ++k) dst[m][k] = *(const PG8_LAS bf16x8*)(lds + PG8_SA(b, h) + aoff + m * 2048 + k * KFR); } while (0)
; #define PG8_LDB(dst, b, h) do { _Pragma("unroll") for (int n = 0; n < 2; ++n) _Pragma("unroll") for (int k = 0; k < 2; ++k) dst[n][k] = *(const PG8_LAS bf16x8*)(lds + PG8_SB(b, h) + boff + n * 2048 + k * KFR); } while (0)
; #define PG8_WAIT_V(n) asm volatile("s_waitcnt vmcnt(" #n ")" ::: "memory")
; #define PG8_WAIT_L(n) asm volatile("s_waitcnt lgkmcnt(" #n ")" ::: "memory")
; #define PG8_BAR __builtin_amdgcn_s_barrier()
; #define PG8_SCHED __builtin_amdgcn_sched_barrier(0)
; template <class Epi, class Sched, bool ALIGN_EPI = false, bool SP2 = false, bool GATHER = false, bool F8 = false>
; __device__ __forceinline__ void gemm_phase(PG8_LAS unsigned char* lds, const Gemm g, const Sched& S, const Epi& E) {
;     ...
;     auto load_gather = [&](const Unit& u, unsigned (&o0)[2], unsigned (&o1)[2]) {
; #pragma unroll
;         for (int i = 0; i < 2; ++i) { int R, C; stage_rc(tid * 16 + i * 8192, R, C); const int t0 = g.gather[u.pm * BM + R], t1 = g.gather[u.pm * BM + HALF + R];
;             o0[i] = (unsigned)(t0 * K + C) * 2u; o1[i] = (unsigned)(t1 * K + C) * 2u; } };
;     ...
;             PG8_LDB(B0, 1, 0); PG8_LDB(B1, 1, 1); PG8_SCHED; PG8_LDA(At, 1, 0); PG8_STAGE_A(PG8_SA(0, 1), a2, 1, last);
;             PG8_WAIT_V(8); PG8_WAIT_L(0); PG8_BAR; PG8_MMA(0, 0, At, B0); PG8_MMA(0, 1, At, B1); PG8_BAR; PG8_SCHED;
;             PG8_LDA(At, 1, 1); PG8_STAGE(PG8_SB(1, 0), b3, voffB); PG8_STAGE(PG8_SB(1, 1), b3 + hstep, voffB); PG8_STAGE_A(PG8_SA(1, 0), a3, 0, last);
;             PG8_WAIT_V(8); PG8_WAIT_L(0); PG8_BAR; PG8_MMA(1, 0, At, B0); PG8_MMA(1, 1, At, B1); PG8_BAR; PG8_SCHED;
	s_add_i32 s64, 0, 0x18000
	s_add_i32 s65, 0, 0x1c000
	v_add_u32_e32 v14, s64, v195
	v_add_u32_e32 v30, s65, v195
	ds_read_b128 v[2:5], v14
	ds_read_b128 v[6:9], v14 offset:16
	ds_read_b128 v[10:13], v14 offset:2048
	ds_read_b128 v[14:17], v14 offset:2064
	ds_read_b128 v[18:21], v30
	ds_read_b128 v[22:25], v30 offset:16
	ds_read_b128 v[26:29], v30 offset:2048
	ds_read_b128 v[30:33], v30 offset:2064
	s_mov_b32 m0, s31
	v_cndmask_b32_e32 v162, v174, v203, vcc
	ds_read_b128 v[206:209], v199 offset:32768
	ds_read_b128 v[210:213], v199 offset:32784
	ds_read_b128 v[214:217], v199 offset:34816
	ds_read_b128 v[218:221], v199 offset:34832
	ds_read_b128 v[228:231], v199 offset:36864
	ds_read_b128 v[232:235], v199 offset:36880
	ds_read_b128 v[236:239], v199 offset:38912
	ds_read_b128 v[240:243], v199 offset:38928
	global_load_lds_dwordx4 v162, s[66:67]
	v_cndmask_b32_e32 v162, v176, v205, vcc
	s_mov_b32 m0, s33
	s_nop 0
	global_load_lds_dwordx4 v162, s[66:67]
	s_waitcnt vmcnt(8)
	s_waitcnt lgkmcnt(0)
	s_barrier
	s_setprio 1
	s_waitcnt lgkmcnt(0)
	v_mfma_scale_f32_16x16x128_f8f6f4 v[158:161], v[2:9], v[206:213], v[158:161], v200, v200 op_sel_hi:[0,0,0]
	v_mfma_scale_f32_16x16x128_f8f6f4 v[154:157], v[10:17], v[206:213], v[154:157], v200, v200 op_sel_hi:[0,0,0]
	v_mfma_scale_f32_16x16x128_f8f6f4 v[142:145], v[2:9], v[214:221], v[142:145], v200, v200 op_sel_hi:[0,0,0]
	v_mfma_scale_f32_16x16x128_f8f6f4 v[134:137], v[10:17], v[214:221], v[134:137], v200, v200 op_sel_hi:[0,0,0]
	v_mfma_scale_f32_16x16x128_f8f6f4 v[126:129], v[2:9], v[228:235], v[126:129], v200, v200 op_sel_hi:[0,0,0]
	v_mfma_scale_f32_16x16x128_f8f6f4 v[118:121], v[10:17], v[228:235], v[118:121], v200, v200 op_sel_hi:[0,0,0]
	v_mfma_scale_f32_16x16x128_f8f6f4 v[110:113], v[2:9], v[236:243], v[110:113], v200, v200 op_sel_hi:[0,0,0]
	v_mfma_scale_f32_16x16x128_f8f6f4 v[102:105], v[10:17], v[236:243], v[102:105], v200, v200 op_sel_hi:[0,0,0]
	s_setprio 0
	s_setprio 1
	v_mfma_scale_f32_16x16x128_f8f6f4 v[150:153], v[18:25], v[206:213], v[150:153], v200, v200 op_sel_hi:[0,0,0]
	v_mfma_scale_f32_16x16x128_f8f6f4 v[146:149], v[26:33], v[206:213], v[146:149], v200, v200 op_sel_hi:[0,0,0]
	v_mfma_scale_f32_16x16x128_f8f6f4 v[138:141], v[18:25], v[214:221], v[138:141], v200, v200 op_sel_hi:[0,0,0]
	v_mfma_scale_f32_16x16x128_f8f6f4 v[130:133], v[26:33], v[214:221], v[130:133], v200, v200 op_sel_hi:[0,0,0]
	v_mfma_scale_f32_16x16x128_f8f6f4 v[122:125], v[18:25], v[228:235], v[122:125], v200, v200 op_sel_hi:[0,0,0]
	v_mfma_scale_f32_16x16x128_f8f6f4 v[114:117], v[26:33], v[228:235], v[114:117], v200, v200 op_sel_hi:[0,0,0]
	v_mfma_scale_f32_16x16x128_f8f6f4 v[106:109], v[18:25], v[236:243], v[106:109], v200, v200 op_sel_hi:[0,0,0]
	v_mfma_scale_f32_16x16x128_f8f6f4 v[98:101], v[26:33], v[236:243], v[98:101], v200, v200 op_sel_hi:[0,0,0]
	s_setprio 0
	s_barrier
	s_add_i32 s64, s64, s25
	v_lshl_add_u64 v[182:183], v[182:183], 0, s[18:19]
	s_mov_b32 m0, s64
	ds_read_b128 v[206:209], v199 offset:49152
	ds_read_b128 v[210:213], v199 offset:49168
	ds_read_b128 v[214:217], v199 offset:51200
	ds_read_b128 v[218:221], v199 offset:51216
	ds_read_b128 v[228:231], v199 offset:53248
	ds_read_b128 v[232:235], v199 offset:53264
	ds_read_b128 v[236:239], v199 offset:55296
	ds_read_b128 v[240:243], v199 offset:55312
	global_load_lds_dwordx4 v[182:183], off
	s_add_i32 m0, s64, 0x2000
	s_add_u32 s62, s62, 0x40080
	v_lshl_add_u64 v[182:183], v[184:185], 0, s[18:19]
	s_addc_u32 s63, s63, 0
	s_add_i32 s64, s65, s25
	global_load_lds_dwordx4 v[182:183], off
	v_lshl_add_u64 v[182:183], s[62:63], 0, v[164:165]
	s_mov_b32 m0, s64
	s_nop 0
	global_load_lds_dwordx4 v[182:183], off
	v_lshl_add_u64 v[182:183], s[62:63], 0, v[166:167]
	s_add_i32 m0, s64, 0x2000
	s_nop 0
	global_load_lds_dwordx4 v[182:183], off
	v_lshl_add_u64 v[182:183], v[186:187], 0, s[18:19]
	s_mov_b32 m0, s69
	s_nop 0
	global_load_lds_dwordx4 v[182:183], off
	v_lshl_add_u64 v[182:183], v[188:189], 0, s[18:19]
	s_mov_b32 m0, s70
	s_nop 0
	global_load_lds_dwordx4 v[182:183], off
	s_waitcnt vmcnt(8)
	v_lshl_or_b32 v202, v248, 11, v192
	v_lshl_or_b32 v203, v249, 11, v192
	v_lshl_or_b32 v204, v250, 11, v193
	v_lshl_or_b32 v205, v251, 11, v193
	s_waitcnt lgkmcnt(0)
	s_barrier
	s_setprio 1
	s_waitcnt lgkmcnt(0)
	v_mfma_scale_f32_16x16x128_f8f6f4 v[94:97], v[2:9], v[206:213], v[94:97], v200, v200 op_sel_hi:[0,0,0]
	v_mfma_scale_f32_16x16x128_f8f6f4 v[86:89], v[10:17], v[206:213], v[86:89], v200, v200 op_sel_hi:[0,0,0]
	v_mfma_scale_f32_16x16x128_f8f6f4 v[78:81], v[2:9], v[214:221], v[78:81], v200, v200 op_sel_hi:[0,0,0]
	v_mfma_scale_f32_16x16x128_f8f6f4 v[70:73], v[10:17], v[214:221], v[70:73], v200, v200 op_sel_hi:[0,0,0]
	v_mfma_scale_f32_16x16x128_f8f6f4 v[62:65], v[2:9], v[228:235], v[62:65], v200, v200 op_sel_hi:[0,0,0]
	v_mfma_scale_f32_16x16x128_f8f6f4 v[54:57], v[10:17], v[228:235], v[54:57], v200, v200 op_sel_hi:[0,0,0]
	v_mfma_scale_f32_16x16x128_f8f6f4 v[46:49], v[2:9], v[236:243], v[46:49], v200, v200 op_sel_hi:[0,0,0]
	v_mfma_scale_f32_16x16x128_f8f6f4 v[38:41], v[10:17], v[236:243], v[38:41], v200, v200 op_sel_hi:[0,0,0]
	s_setprio 0
	s_setprio 1
	v_mfma_scale_f32_16x16x128_f8f6f4 v[90:93], v[18:25], v[206:213], v[90:93], v200, v200 op_sel_hi:[0,0,0]
	v_mfma_scale_f32_16x16x128_f8f6f4 v[82:85], v[26:33], v[206:213], v[82:85], v200, v200 op_sel_hi:[0,0,0]
	v_mfma_scale_f32_16x16x128_f8f6f4 v[74:77], v[18:25], v[214:221], v[74:77], v200, v200 op_sel_hi:[0,0,0]
	v_mfma_scale_f32_16x16x128_f8f6f4 v[66:69], v[26:33], v[214:221], v[66:69], v200, v200 op_sel_hi:[0,0,0]
	v_mfma_scale_f32_16x16x128_f8f6f4 v[58:61], v[18:25], v[228:235], v[58:61], v200, v200 op_sel_hi:[0,0,0]
	v_mfma_scale_f32_16x16x128_f8f6f4 v[50:53], v[26:33], v[228:235], v[50:53], v200, v200 op_sel_hi:[0,0,0]
	v_mfma_scale_f32_16x16x128_f8f6f4 v[42:45], v[18:25], v[236:243], v[42:45], v200, v200 op_sel_hi:[0,0,0]
	v_mfma_scale_f32_16x16x128_f8f6f4 v[34:37], v[26:33], v[236:243], v[34:37], v200, v200 op_sel_hi:[0,0,0]
	s_setprio 0
	s_barrier
	s_add_i32 s77, s77, 2
	s_cmp_gt_u32 s77, 13
	s_mov_b64 s[64:65], s[4:5]
	s_cbranch_scc0 .LBB0_1386
	s_and_b64 vcc, exec, s[22:23]
	s_cbranch_vccz .LBB0_1389
	s_barrier
